# final output stores issued at agent scope (write-through): no dirty output lines left in the L2 during the gather or at kernel end
# speedup vs baseline: 1.0093x; 1.0047x over previous
; DI void peer_token(LAS unsigned char* ring, const bf16* x1row, float inv2, const float* nffn, const int* ex, const float* pg, const unsigned char* U6, const unsigned char* V6,
;                    const float* usc, const float* vsc, float* orow, int lane) {
;     ...
;     const float ysc = 1.0f;
;     asm volatile("s_waitcnt vmcnt(0)" ::: "memory");
; #pragma unroll
;     for (int i = 0; i < 16; ++i) {
;         const v2u aw = *(const v2u*)(x1row + i * 256 + lane * 4);
;         *(f32x4*)(orow + i * 256 + lane * 4) = (f32x4){bflo(aw.x) + ysc * y[2 * i].x, bfhi(aw.x) + ysc * y[2 * i].y, bflo(aw.y) + ysc * y[2 * i + 1].x, bfhi(aw.y) + ysc * y[2 * i + 1].y};
;     }
.Lpvt9E:
	s_lshl_b32 s46, s76, 1
	s_add_i32 s46, s46, s97
	s_ashr_i32 s47, s46, 31
	s_lshl_b64 s[46:47], s[46:47], 13
	v_lshl_add_u64 v[16:17], v[68:69], 0, s[46:47]
	s_mov_b64 s[46:47], 0x2000
	v_lshl_add_u64 v[2:3], v[16:17], 0, s[46:47]
	s_mov_b64 s[46:47], 0x3000
	v_lshl_add_u64 v[4:5], v[16:17], 0, s[46:47]
	global_load_dwordx2 v[98:99], v[2:3], off
	global_load_dwordx2 v[100:101], v[2:3], off offset:512
	global_load_dwordx2 v[102:103], v[2:3], off offset:1024
	global_load_dwordx2 v[104:105], v[2:3], off offset:1536
	global_load_dwordx2 v[126:127], v[2:3], off offset:2048
	global_load_dwordx2 v[128:129], v[2:3], off offset:2560
	global_load_dwordx2 v[130:131], v[2:3], off offset:3072
	global_load_dwordx2 v[132:133], v[2:3], off offset:3584
	global_load_dwordx2 v[136:137], v[4:5], off
	global_load_dwordx2 v[138:139], v[4:5], off offset:512
	global_load_dwordx2 v[140:141], v[4:5], off offset:1024
	global_load_dwordx2 v[142:143], v[4:5], off offset:1536
	global_load_dwordx2 v[8:9], v[4:5], off offset:2048
	global_load_dwordx2 v[10:11], v[4:5], off offset:2560
	global_load_dwordx2 v[12:13], v[4:5], off offset:3072
	global_load_dwordx2 v[14:15], v[4:5], off offset:3584
	v_lshl_add_u64 v[18:19], s[44:45], 2, v[76:77]
	s_mov_b64 s[46:47], 0x2000
	v_lshl_add_u64 v[6:7], v[18:19], 0, s[46:47]
	s_mov_b64 s[46:47], 0x3000
	v_lshl_add_u64 v[16:17], v[18:19], 0, s[46:47]
	s_mov_b64 s[46:47], 0x4000
	v_lshl_add_u64 v[112:113], v[18:19], 0, s[46:47]
	s_mov_b64 s[46:47], 0x6000
	v_lshl_add_u64 v[242:243], v[18:19], 0, s[46:47]
	s_mov_b64 s[46:47], 0x7000
	v_lshl_add_u64 v[124:125], v[18:19], 0, s[46:47]
	v_lshlrev_b32_e32 v2, 16, v146
	v_and_b32_e32 v3, 0xffff0000, v146
	v_lshlrev_b32_e32 v4, 16, v147
	v_and_b32_e32 v5, 0xffff0000, v147
	v_pk_add_f32 v[2:3], v[94:95], v[2:3]
	v_pk_add_f32 v[4:5], v[96:97], v[4:5]
	global_store_dwordx4 v[18:19], v[2:5], off sc1
	v_lshlrev_b32_e32 v244, 16, v148
	v_and_b32_e32 v245, 0xffff0000, v148
	v_lshlrev_b32_e32 v246, 16, v149
	v_and_b32_e32 v247, 0xffff0000, v149
	v_pk_add_f32 v[244:245], v[92:93], v[244:245]
	v_pk_add_f32 v[246:247], v[90:91], v[246:247]
	global_store_dwordx4 v[18:19], v[244:247], off offset:1024 sc1
	v_lshlrev_b32_e32 v120, 16, v150
	v_and_b32_e32 v121, 0xffff0000, v150
	v_lshlrev_b32_e32 v122, 16, v151
	v_and_b32_e32 v123, 0xffff0000, v151
	v_pk_add_f32 v[120:121], v[88:89], v[120:121]
	v_pk_add_f32 v[122:123], v[86:87], v[122:123]
	global_store_dwordx4 v[18:19], v[120:123], off offset:2048 sc1
	v_lshlrev_b32_e32 v2, 16, v152
	v_and_b32_e32 v3, 0xffff0000, v152
	v_lshlrev_b32_e32 v4, 16, v153
	v_and_b32_e32 v5, 0xffff0000, v153
	v_pk_add_f32 v[2:3], v[84:85], v[2:3]
	v_pk_add_f32 v[4:5], v[82:83], v[4:5]
	global_store_dwordx4 v[18:19], v[2:5], off offset:3072 sc1
	v_lshlrev_b32_e32 v244, 16, v154
	v_and_b32_e32 v245, 0xffff0000, v154
	v_lshlrev_b32_e32 v246, 16, v155
	v_and_b32_e32 v247, 0xffff0000, v155
	v_pk_add_f32 v[244:245], v[64:65], v[244:245]
	v_pk_add_f32 v[246:247], v[80:81], v[246:247]
	global_store_dwordx4 v[6:7], v[244:247], off offset:-4096 sc1
	v_lshlrev_b32_e32 v120, 16, v156
	v_and_b32_e32 v121, 0xffff0000, v156
	v_lshlrev_b32_e32 v122, 16, v157
	v_and_b32_e32 v123, 0xffff0000, v157
	v_pk_add_f32 v[120:121], v[62:63], v[120:121]
	v_pk_add_f32 v[122:123], v[60:61], v[122:123]
	global_store_dwordx4 v[6:7], v[120:123], off offset:-3072 sc1
	v_lshlrev_b32_e32 v2, 16, v158
	v_and_b32_e32 v3, 0xffff0000, v158
	v_lshlrev_b32_e32 v4, 16, v159
	v_and_b32_e32 v5, 0xffff0000, v159
	v_pk_add_f32 v[2:3], v[58:59], v[2:3]
	v_pk_add_f32 v[4:5], v[56:57], v[4:5]
	global_store_dwordx4 v[6:7], v[2:5], off offset:-2048 sc1
	v_lshlrev_b32_e32 v244, 16, v160
	v_and_b32_e32 v245, 0xffff0000, v160
	v_lshlrev_b32_e32 v246, 16, v161
	v_and_b32_e32 v247, 0xffff0000, v161
	v_pk_add_f32 v[244:245], v[54:55], v[244:245]
	v_pk_add_f32 v[246:247], v[52:53], v[246:247]
	global_store_dwordx4 v[6:7], v[244:247], off offset:-1024 sc1
	v_lshlrev_b32_e32 v120, 16, v162
	v_and_b32_e32 v121, 0xffff0000, v162
	v_lshlrev_b32_e32 v122, 16, v163
	v_and_b32_e32 v123, 0xffff0000, v163
	v_pk_add_f32 v[120:121], v[50:51], v[120:121]
	v_pk_add_f32 v[122:123], v[48:49], v[122:123]
	global_store_dwordx4 v[6:7], v[120:123], off sc1
	v_lshlrev_b32_e32 v2, 16, v164
	v_and_b32_e32 v3, 0xffff0000, v164
	v_lshlrev_b32_e32 v4, 16, v165
	v_and_b32_e32 v5, 0xffff0000, v165
	v_pk_add_f32 v[2:3], v[46:47], v[2:3]
	v_pk_add_f32 v[4:5], v[44:45], v[4:5]
	global_store_dwordx4 v[6:7], v[2:5], off offset:1024 sc1
	v_lshlrev_b32_e32 v244, 16, v166
	v_and_b32_e32 v245, 0xffff0000, v166
	v_lshlrev_b32_e32 v246, 16, v167
	v_and_b32_e32 v247, 0xffff0000, v167
	v_pk_add_f32 v[244:245], v[42:43], v[244:245]
	v_pk_add_f32 v[246:247], v[40:41], v[246:247]
	global_store_dwordx4 v[6:7], v[244:247], off offset:2048 sc1
	v_lshlrev_b32_e32 v120, 16, v168
	v_and_b32_e32 v121, 0xffff0000, v168
	v_lshlrev_b32_e32 v122, 16, v169
	v_and_b32_e32 v123, 0xffff0000, v169
	v_pk_add_f32 v[120:121], v[38:39], v[120:121]
	v_pk_add_f32 v[122:123], v[36:37], v[122:123]
	global_store_dwordx4 v[6:7], v[120:123], off offset:3072 sc1
	v_lshlrev_b32_e32 v2, 16, v170
	v_and_b32_e32 v3, 0xffff0000, v170
	v_lshlrev_b32_e32 v4, 16, v171
	v_and_b32_e32 v5, 0xffff0000, v171
	v_pk_add_f32 v[2:3], v[32:33], v[2:3]
	v_pk_add_f32 v[4:5], v[34:35], v[4:5]
	global_store_dwordx4 v[16:17], v[2:5], off sc1
	v_lshlrev_b32_e32 v244, 16, v172
	v_and_b32_e32 v245, 0xffff0000, v172
	v_lshlrev_b32_e32 v246, 16, v173
	v_and_b32_e32 v247, 0xffff0000, v173
	v_pk_add_f32 v[244:245], v[30:31], v[244:245]
	v_pk_add_f32 v[246:247], v[28:29], v[246:247]
	global_store_dwordx4 v[16:17], v[244:247], off offset:1024 sc1
	v_lshlrev_b32_e32 v120, 16, v174
	v_and_b32_e32 v121, 0xffff0000, v174
	v_lshlrev_b32_e32 v122, 16, v175
	v_and_b32_e32 v123, 0xffff0000, v175
	v_pk_add_f32 v[120:121], v[26:27], v[120:121]
	v_pk_add_f32 v[122:123], v[24:25], v[122:123]
	global_store_dwordx4 v[16:17], v[120:123], off offset:2048 sc1
	v_lshlrev_b32_e32 v2, 16, v176
	v_and_b32_e32 v3, 0xffff0000, v176
	v_lshlrev_b32_e32 v4, 16, v177
	v_and_b32_e32 v5, 0xffff0000, v177
	v_pk_add_f32 v[2:3], v[20:21], v[2:3]
	v_pk_add_f32 v[4:5], v[22:23], v[4:5]
	global_store_dwordx4 v[16:17], v[2:5], off offset:3072 sc1
	s_waitcnt vmcnt(16)
; DI void peer_token(LAS unsigned char* ring, const bf16* x1row, float inv2, const float* nffn, const int* ex, const float* pg, const unsigned char* U6, const unsigned char* V6,
;                    const float* usc, const float* vsc, float* orow, int lane) {
;     ...
;     const float ysc = 1.0f;
;     asm volatile("s_waitcnt vmcnt(0)" ::: "memory");
; #pragma unroll
;     for (int i = 0; i < 16; ++i) {
;         const v2u aw = *(const v2u*)(x1row + i * 256 + lane * 4);
;         *(f32x4*)(orow + i * 256 + lane * 4) = (f32x4){bflo(aw.x) + ysc * y[2 * i].x, bfhi(aw.x) + ysc * y[2 * i].y, bflo(aw.y) + ysc * y[2 * i + 1].x, bfhi(aw.y) + ysc * y[2 * i + 1].y};
;     }
	v_lshlrev_b32_e32 v244, 16, v98
	v_and_b32_e32 v245, 0xffff0000, v98
	v_lshlrev_b32_e32 v246, 16, v99
	v_and_b32_e32 v247, 0xffff0000, v99
	v_pk_add_f32 v[244:245], v[178:179], v[244:245]
	v_pk_add_f32 v[246:247], v[180:181], v[246:247]
	global_store_dwordx4 v[112:113], v[244:247], off sc1
	v_lshlrev_b32_e32 v120, 16, v100
	v_and_b32_e32 v121, 0xffff0000, v100
	v_lshlrev_b32_e32 v122, 16, v101
	v_and_b32_e32 v123, 0xffff0000, v101
	v_pk_add_f32 v[120:121], v[182:183], v[120:121]
	v_pk_add_f32 v[122:123], v[184:185], v[122:123]
	global_store_dwordx4 v[112:113], v[120:123], off offset:1024 sc1
	v_lshlrev_b32_e32 v2, 16, v102
	v_and_b32_e32 v3, 0xffff0000, v102
	v_lshlrev_b32_e32 v4, 16, v103
	v_and_b32_e32 v5, 0xffff0000, v103
	v_pk_add_f32 v[2:3], v[186:187], v[2:3]
	v_pk_add_f32 v[4:5], v[188:189], v[4:5]
	global_store_dwordx4 v[112:113], v[2:5], off offset:2048 sc1
	v_lshlrev_b32_e32 v244, 16, v104
	v_and_b32_e32 v245, 0xffff0000, v104
	v_lshlrev_b32_e32 v246, 16, v105
	v_and_b32_e32 v247, 0xffff0000, v105
	v_pk_add_f32 v[244:245], v[190:191], v[244:245]
	v_pk_add_f32 v[246:247], v[192:193], v[246:247]
	global_store_dwordx4 v[112:113], v[244:247], off offset:3072 sc1
	v_lshlrev_b32_e32 v120, 16, v126
	v_and_b32_e32 v121, 0xffff0000, v126
	v_lshlrev_b32_e32 v122, 16, v127
	v_and_b32_e32 v123, 0xffff0000, v127
	v_pk_add_f32 v[120:121], v[194:195], v[120:121]
	v_pk_add_f32 v[122:123], v[196:197], v[122:123]
	global_store_dwordx4 v[242:243], v[120:123], off offset:-4096 sc1
	v_lshlrev_b32_e32 v2, 16, v128
	v_and_b32_e32 v3, 0xffff0000, v128
	v_lshlrev_b32_e32 v4, 16, v129
	v_and_b32_e32 v5, 0xffff0000, v129
	v_pk_add_f32 v[2:3], v[198:199], v[2:3]
	v_pk_add_f32 v[4:5], v[200:201], v[4:5]
	global_store_dwordx4 v[242:243], v[2:5], off offset:-3072 sc1
	v_lshlrev_b32_e32 v244, 16, v130
	v_and_b32_e32 v245, 0xffff0000, v130
	v_lshlrev_b32_e32 v246, 16, v131
	v_and_b32_e32 v247, 0xffff0000, v131
	v_pk_add_f32 v[244:245], v[202:203], v[244:245]
	v_pk_add_f32 v[246:247], v[204:205], v[246:247]
	global_store_dwordx4 v[242:243], v[244:247], off offset:-2048 sc1
	v_lshlrev_b32_e32 v120, 16, v132
	v_and_b32_e32 v121, 0xffff0000, v132
	v_lshlrev_b32_e32 v122, 16, v133
	v_and_b32_e32 v123, 0xffff0000, v133
	v_pk_add_f32 v[120:121], v[206:207], v[120:121]
	v_pk_add_f32 v[122:123], v[208:209], v[122:123]
	global_store_dwordx4 v[242:243], v[120:123], off offset:-1024 sc1
	v_lshlrev_b32_e32 v2, 16, v136
	v_and_b32_e32 v3, 0xffff0000, v136
	v_lshlrev_b32_e32 v4, 16, v137
	v_and_b32_e32 v5, 0xffff0000, v137
	v_pk_add_f32 v[2:3], v[210:211], v[2:3]
	v_pk_add_f32 v[4:5], v[212:213], v[4:5]
	global_store_dwordx4 v[242:243], v[2:5], off sc1
	v_lshlrev_b32_e32 v244, 16, v138
	v_and_b32_e32 v245, 0xffff0000, v138
	v_lshlrev_b32_e32 v246, 16, v139
	v_and_b32_e32 v247, 0xffff0000, v139
	v_pk_add_f32 v[244:245], v[214:215], v[244:245]
	v_pk_add_f32 v[246:247], v[216:217], v[246:247]
	global_store_dwordx4 v[242:243], v[244:247], off offset:1024 sc1
	v_lshlrev_b32_e32 v120, 16, v140
	v_and_b32_e32 v121, 0xffff0000, v140
	v_lshlrev_b32_e32 v122, 16, v141
	v_and_b32_e32 v123, 0xffff0000, v141
	v_pk_add_f32 v[120:121], v[218:219], v[120:121]
	v_pk_add_f32 v[122:123], v[220:221], v[122:123]
	global_store_dwordx4 v[242:243], v[120:123], off offset:2048 sc1
	v_lshlrev_b32_e32 v2, 16, v142
	v_and_b32_e32 v3, 0xffff0000, v142
	v_lshlrev_b32_e32 v4, 16, v143
	v_and_b32_e32 v5, 0xffff0000, v143
	v_pk_add_f32 v[2:3], v[222:223], v[2:3]
	v_pk_add_f32 v[4:5], v[224:225], v[4:5]
	global_store_dwordx4 v[242:243], v[2:5], off offset:3072 sc1
	v_lshlrev_b32_e32 v244, 16, v8
	v_and_b32_e32 v245, 0xffff0000, v8
	v_lshlrev_b32_e32 v246, 16, v9
	v_and_b32_e32 v247, 0xffff0000, v9
	v_pk_add_f32 v[244:245], v[226:227], v[244:245]
	v_pk_add_f32 v[246:247], v[228:229], v[246:247]
	global_store_dwordx4 v[124:125], v[244:247], off sc1
	v_lshlrev_b32_e32 v120, 16, v10
	v_and_b32_e32 v121, 0xffff0000, v10
	v_lshlrev_b32_e32 v122, 16, v11
	v_and_b32_e32 v123, 0xffff0000, v11
	v_pk_add_f32 v[120:121], v[230:231], v[120:121]
	v_pk_add_f32 v[122:123], v[232:233], v[122:123]
	global_store_dwordx4 v[124:125], v[120:123], off offset:1024 sc1
	v_lshlrev_b32_e32 v2, 16, v12
	v_and_b32_e32 v3, 0xffff0000, v12
	v_lshlrev_b32_e32 v4, 16, v13
	v_and_b32_e32 v5, 0xffff0000, v13
	v_pk_add_f32 v[2:3], v[234:235], v[2:3]
	v_pk_add_f32 v[4:5], v[236:237], v[4:5]
	global_store_dwordx4 v[124:125], v[2:5], off offset:2048 sc1
	v_lshlrev_b32_e32 v244, 16, v14
	v_and_b32_e32 v245, 0xffff0000, v14
	v_lshlrev_b32_e32 v246, 16, v15
	v_and_b32_e32 v247, 0xffff0000, v15
	v_pk_add_f32 v[244:245], v[238:239], v[244:245]
	v_pk_add_f32 v[246:247], v[240:241], v[246:247]
	global_store_dwordx4 v[124:125], v[244:247], off offset:3072 sc1
	s_add_i32 s76, s76, 1
	s_cmp_eq_u32 s76, 2
	s_cbranch_scc0 .LBB0_901
	s_add_i32 s2, s2, s3
	s_cmpk_gt_i32 s2, 0xff
	s_barrier
	s_cbranch_scc0 .LBB0_892
